# batch2: + P11 routing-record wait moved behind the row loads, moe tables built once, expert search by ballot, P9/P10 bias loads hoisted (no sc1)
# speedup vs baseline: 1.0141x; 1.0141x over previous
.LBB0_1101:
	v_lshlrev_b32_e32 v48, 2, v48
	v_add_u32_e32 v48, s9, v48
	global_load_dwordx4 v[60:63], v[70:71], off
	global_load_dwordx4 v[56:59], v[70:71], off offset:1024
	global_load_dwordx4 v[52:55], v[70:71], off offset:2048
	global_load_dwordx4 v[40:43], v[70:71], off offset:3072
	ds_read_b32 v64, v48 offset:64
	s_ashr_i32 s31, s4, 31
	s_mov_b32 s30, s4
	s_lshl_b64 s[30:31], s[30:31], 11
	v_lshlrev_b32_e32 v48, 2, v49
	s_waitcnt lgkmcnt(0)
	v_lshlrev_b64 v[80:81], 19, v[64:65]
	v_lshl_add_u64 v[80:81], s[10:11], 0, v[80:81]
	v_lshl_add_u64 v[80:81], v[80:81], 0, s[30:31]
	v_lshl_add_u64 v[80:81], v[80:81], 0, v[66:67]
	v_add_u32_e32 v48, s9, v48
	global_load_dwordx2 v[82:83], v[80:81], off
	global_load_dwordx2 v[84:85], v[80:81], off offset:512
	global_load_dwordx2 v[86:87], v[80:81], off offset:1024
	global_load_dwordx2 v[88:89], v[80:81], off offset:1536
	ds_read_b32 v64, v48 offset:64
	s_ashr_i32 s31, s5, 31
	s_mov_b32 s30, s5
	s_lshl_b64 s[4:5], s[30:31], 11
	v_lshlrev_b32_e32 v50, 2, v50
	s_waitcnt lgkmcnt(0)
	v_lshlrev_b64 v[48:49], 19, v[64:65]
	v_lshl_add_u64 v[48:49], s[10:11], 0, v[48:49]
	v_lshl_add_u64 v[48:49], v[48:49], 0, s[4:5]
	v_lshl_add_u64 v[48:49], v[48:49], 0, v[66:67]
	v_add_u32_e32 v50, s9, v50
	global_load_dwordx2 v[80:81], v[48:49], off
	global_load_dwordx2 v[90:91], v[48:49], off offset:512
	global_load_dwordx2 v[92:93], v[48:49], off offset:1024
	global_load_dwordx2 v[94:95], v[48:49], off offset:1536
	ds_read_b32 v64, v50 offset:64
	s_ashr_i32 s5, s6, 31
	s_mov_b32 s4, s6
	s_lshl_b64 s[4:5], s[4:5], 11
	v_lshlrev_b32_e32 v50, 2, v51
	s_waitcnt lgkmcnt(0)
	v_lshlrev_b64 v[48:49], 19, v[64:65]
	v_lshl_add_u64 v[48:49], s[10:11], 0, v[48:49]
	v_lshl_add_u64 v[48:49], v[48:49], 0, s[4:5]
	v_lshl_add_u64 v[48:49], v[48:49], 0, v[66:67]
	v_add_u32_e32 v64, s9, v50
	global_load_dwordx2 v[96:97], v[48:49], off
	global_load_dwordx2 v[50:51], v[48:49], off offset:512
	global_load_dwordx2 v[98:99], v[48:49], off offset:1024
	global_load_dwordx2 v[100:101], v[48:49], off offset:1536
	ds_read_b32 v64, v64 offset:64
	s_ashr_i32 s5, s7, 31
	s_mov_b32 s4, s7
	s_lshl_b64 s[4:5], s[4:5], 11
	v_mul_f32_e32 v44, 0x3e000000, v44
	s_waitcnt lgkmcnt(0)
	v_lshlrev_b64 v[48:49], 19, v[64:65]
	v_lshl_add_u64 v[48:49], s[10:11], 0, v[48:49]
	v_lshl_add_u64 v[48:49], v[48:49], 0, s[4:5]
	v_lshl_add_u64 v[48:49], v[48:49], 0, v[66:67]
	global_load_dwordx2 v[102:103], v[48:49], off
	global_load_dwordx2 v[104:105], v[48:49], off offset:512
	global_load_dwordx2 v[106:107], v[48:49], off offset:1024
	global_load_dwordx2 v[108:109], v[48:49], off offset:1536
	v_mul_f32_e32 v48, 0x3e000000, v45
	v_mul_f32_e32 v46, 0x3e000000, v46
	v_mul_f32_e32 v64, 0x3e000000, v47
	s_waitcnt vmcnt(22)
	v_readfirstlane_b32 s0, v208
	v_readfirstlane_b32 s1, v209
	v_readfirstlane_b32 s2, v210
	v_readfirstlane_b32 s3, v211
	s_mov_b64 s[6:7], s[2:3]
	s_add_i32 s16, s16, s29
	v_lshl_add_u64 v[70:71], v[70:71], 0, s[18:19]
	s_mov_b64 s[4:5], s[0:1]
	s_waitcnt vmcnt(19)
	v_lshlrev_b32_e32 v206, 16, v60
	v_and_b32_e32 v207, 0xffff0000, v60
	v_lshlrev_b32_e32 v60, 16, v61
	v_and_b32_e32 v61, 0xffff0000, v61
	s_waitcnt vmcnt(15)
	v_cvt_pk_f32_fp8_sdwa v[112:113], v82 src0_sel:WORD_1
	v_cvt_pk_f32_fp8_e32 v[110:111], v82
	v_cvt_pk_f32_fp8_e32 v[114:115], v83
	v_cvt_pk_f32_fp8_sdwa v[82:83], v83 src0_sel:WORD_1
	s_waitcnt vmcnt(14)
	v_cvt_pk_f32_fp8_e32 v[116:117], v84
	v_cvt_pk_f32_fp8_e32 v[120:121], v85
	v_pk_fma_f32 v[60:61], v[44:45], v[112:113], v[60:61] op_sel_hi:[0,1,1]
	v_cvt_pk_f32_fp8_sdwa v[118:119], v84 src0_sel:WORD_1
	v_cvt_pk_f32_fp8_sdwa v[84:85], v85 src0_sel:WORD_1
	s_waitcnt vmcnt(13)
	v_cvt_pk_f32_fp8_e32 v[122:123], v86
	v_cvt_pk_f32_fp8_sdwa v[124:125], v86 src0_sel:WORD_1
	v_cvt_pk_f32_fp8_e32 v[126:127], v87
	v_cvt_pk_f32_fp8_sdwa v[86:87], v87 src0_sel:WORD_1
	s_waitcnt vmcnt(12)
	v_cvt_pk_f32_fp8_e32 v[128:129], v88
	s_waitcnt vmcnt(11)
	v_cvt_pk_f32_fp8_sdwa v[136:137], v80 src0_sel:WORD_1
	v_cvt_pk_f32_fp8_e32 v[134:135], v80
	s_waitcnt vmcnt(9)
	v_cvt_pk_f32_fp8_e32 v[146:147], v92
	v_cvt_pk_f32_fp8_sdwa v[148:149], v92 src0_sel:WORD_1
	v_pk_fma_f32 v[60:61], v[48:49], v[136:137], v[60:61] op_sel_hi:[0,1,1]
	v_lshlrev_b32_e32 v136, 16, v62
	v_and_b32_e32 v137, 0xffff0000, v62
	v_lshlrev_b32_e32 v62, 16, v63
	v_and_b32_e32 v63, 0xffff0000, v63
	v_cvt_pk_f32_fp8_e32 v[150:151], v93
	v_cvt_pk_f32_fp8_sdwa v[92:93], v93 src0_sel:WORD_1
	v_pk_fma_f32 v[62:63], v[44:45], v[82:83], v[62:63] op_sel_hi:[0,1,1]
	s_waitcnt vmcnt(7)
	v_cvt_pk_f32_fp8_e32 v[158:159], v96
	v_lshlrev_b32_e32 v82, 16, v56
	v_and_b32_e32 v83, 0xffff0000, v56
	v_cvt_pk_f32_fp8_sdwa v[130:131], v88 src0_sel:WORD_1
	v_cvt_pk_f32_fp8_e32 v[132:133], v89
	v_cvt_pk_f32_fp8_sdwa v[88:89], v89 src0_sel:WORD_1
	v_cvt_pk_f32_fp8_sdwa v[160:161], v96 src0_sel:WORD_1
	v_pk_fma_f32 v[82:83], v[44:45], v[116:117], v[82:83] op_sel_hi:[0,1,1]
	s_waitcnt vmcnt(3)
	v_cvt_pk_f32_fp8_e32 v[182:183], v102
	v_lshlrev_b32_e32 v116, 16, v58
	v_and_b32_e32 v117, 0xffff0000, v58
	v_cvt_pk_f32_fp8_e32 v[138:139], v81
	v_cvt_pk_f32_fp8_sdwa v[80:81], v81 src0_sel:WORD_1
	v_cvt_pk_f32_fp8_e32 v[140:141], v90
	v_cvt_pk_f32_fp8_sdwa v[142:143], v90 src0_sel:WORD_1
	v_cvt_pk_f32_fp8_e32 v[144:145], v91
	v_cvt_pk_f32_fp8_sdwa v[90:91], v91 src0_sel:WORD_1
	v_cvt_pk_f32_fp8_e32 v[152:153], v94
	v_cvt_pk_f32_fp8_sdwa v[154:155], v94 src0_sel:WORD_1
	v_cvt_pk_f32_fp8_e32 v[156:157], v95
	v_cvt_pk_f32_fp8_sdwa v[94:95], v95 src0_sel:WORD_1
	v_cvt_pk_f32_fp8_sdwa v[184:185], v102 src0_sel:WORD_1
	v_pk_fma_f32 v[110:111], v[44:45], v[110:111], v[206:207] op_sel_hi:[0,1,1]
	v_pk_fma_f32 v[116:117], v[44:45], v[120:121], v[116:117] op_sel_hi:[0,1,1]
	v_lshlrev_b32_e32 v58, 16, v59
	v_and_b32_e32 v59, 0xffff0000, v59
	v_lshlrev_b32_e32 v120, 16, v54
	v_and_b32_e32 v121, 0xffff0000, v54
	v_lshlrev_b32_e32 v54, 16, v55
	v_and_b32_e32 v55, 0xffff0000, v55
	v_cvt_pk_f32_fp8_e32 v[162:163], v97
	v_cvt_pk_f32_fp8_sdwa v[96:97], v97 src0_sel:WORD_1
	v_cvt_pk_f32_fp8_e32 v[164:165], v50
	v_cvt_pk_f32_fp8_sdwa v[166:167], v50 src0_sel:WORD_1
	v_cvt_pk_f32_fp8_e32 v[168:169], v51
	v_cvt_pk_f32_fp8_sdwa v[50:51], v51 src0_sel:WORD_1
	v_cvt_pk_f32_fp8_e32 v[170:171], v98
	v_cvt_pk_f32_fp8_sdwa v[172:173], v98 src0_sel:WORD_1
	v_cvt_pk_f32_fp8_e32 v[174:175], v99
	v_cvt_pk_f32_fp8_sdwa v[98:99], v99 src0_sel:WORD_1
	v_cvt_pk_f32_fp8_e32 v[176:177], v100
	v_cvt_pk_f32_fp8_sdwa v[178:179], v100 src0_sel:WORD_1
	v_cvt_pk_f32_fp8_e32 v[180:181], v101
	v_cvt_pk_f32_fp8_sdwa v[100:101], v101 src0_sel:WORD_1
	v_pk_fma_f32 v[110:111], v[48:49], v[134:135], v[110:111] op_sel_hi:[0,1,1]
	v_pk_fma_f32 v[58:59], v[44:45], v[84:85], v[58:59] op_sel_hi:[0,1,1]
	v_lshlrev_b32_e32 v84, 16, v52
	v_and_b32_e32 v85, 0xffff0000, v52
	v_lshlrev_b32_e32 v52, 16, v53
	v_and_b32_e32 v53, 0xffff0000, v53
	v_pk_fma_f32 v[54:55], v[44:45], v[86:87], v[54:55] op_sel_hi:[0,1,1]
	v_cvt_pk_f32_fp8_e32 v[186:187], v103
	v_pk_fma_f32 v[110:111], v[46:47], v[158:159], v[110:111] op_sel_hi:[0,1,1]
	v_lshlrev_b32_e32 v56, 16, v57
	v_and_b32_e32 v57, 0xffff0000, v57
	v_pk_fma_f32 v[52:53], v[44:45], v[124:125], v[52:53] op_sel_hi:[0,1,1]
	v_pk_fma_f32 v[54:55], v[48:49], v[92:93], v[54:55] op_sel_hi:[0,1,1]
	v_lshlrev_b32_e32 v92, 16, v40
	v_and_b32_e32 v93, 0xffff0000, v40
	v_lshlrev_b32_e32 v40, 16, v41
	v_and_b32_e32 v41, 0xffff0000, v41
	v_lshlrev_b32_e32 v124, 16, v42
	v_and_b32_e32 v125, 0xffff0000, v42
	v_lshlrev_b32_e32 v42, 16, v43
	v_and_b32_e32 v43, 0xffff0000, v43
	v_pk_fma_f32 v[110:111], v[64:65], v[182:183], v[110:111] op_sel_hi:[0,1,1]
	v_pk_fma_f32 v[60:61], v[46:47], v[160:161], v[60:61] op_sel_hi:[0,1,1]
	v_pk_fma_f32 v[114:115], v[44:45], v[114:115], v[136:137] op_sel_hi:[0,1,1]
	v_pk_fma_f32 v[56:57], v[44:45], v[118:119], v[56:57] op_sel_hi:[0,1,1]
	v_pk_fma_f32 v[84:85], v[44:45], v[122:123], v[84:85] op_sel_hi:[0,1,1]
	v_pk_fma_f32 v[120:121], v[44:45], v[126:127], v[120:121] op_sel_hi:[0,1,1]
	v_pk_fma_f32 v[92:93], v[44:45], v[128:129], v[92:93] op_sel_hi:[0,1,1]
	v_pk_fma_f32 v[40:41], v[44:45], v[130:131], v[40:41] op_sel_hi:[0,1,1]
	v_pk_fma_f32 v[124:125], v[44:45], v[132:133], v[124:125] op_sel_hi:[0,1,1]
	v_pk_fma_f32 v[42:43], v[44:45], v[88:89], v[42:43] op_sel_hi:[0,1,1]
	v_cvt_pk_f32_fp8_sdwa v[102:103], v103 src0_sel:WORD_1
	v_pk_mul_f32 v[134:135], v[110:111], v[110:111]
	v_pk_fma_f32 v[60:61], v[64:65], v[184:185], v[60:61] op_sel_hi:[0,1,1]
	v_pk_fma_f32 v[114:115], v[48:49], v[138:139], v[114:115] op_sel_hi:[0,1,1]
	v_pk_fma_f32 v[62:63], v[48:49], v[80:81], v[62:63] op_sel_hi:[0,1,1]
	v_pk_fma_f32 v[82:83], v[48:49], v[140:141], v[82:83] op_sel_hi:[0,1,1]
	v_pk_fma_f32 v[56:57], v[48:49], v[142:143], v[56:57] op_sel_hi:[0,1,1]
	v_pk_fma_f32 v[116:117], v[48:49], v[144:145], v[116:117] op_sel_hi:[0,1,1]
	v_pk_fma_f32 v[58:59], v[48:49], v[90:91], v[58:59] op_sel_hi:[0,1,1]
	v_pk_fma_f32 v[84:85], v[48:49], v[146:147], v[84:85] op_sel_hi:[0,1,1]
	v_pk_fma_f32 v[52:53], v[48:49], v[148:149], v[52:53] op_sel_hi:[0,1,1]
	v_pk_fma_f32 v[120:121], v[48:49], v[150:151], v[120:121] op_sel_hi:[0,1,1]
	v_pk_fma_f32 v[92:93], v[48:49], v[152:153], v[92:93] op_sel_hi:[0,1,1]
	v_pk_fma_f32 v[40:41], v[48:49], v[154:155], v[40:41] op_sel_hi:[0,1,1]
	v_pk_fma_f32 v[124:125], v[48:49], v[156:157], v[124:125] op_sel_hi:[0,1,1]
	v_pk_fma_f32 v[42:43], v[48:49], v[94:95], v[42:43] op_sel_hi:[0,1,1]
	v_pk_mul_f32 v[112:113], v[60:61], v[60:61]
	v_pk_fma_f32 v[114:115], v[46:47], v[162:163], v[114:115] op_sel_hi:[0,1,1]
	v_pk_fma_f32 v[62:63], v[46:47], v[96:97], v[62:63] op_sel_hi:[0,1,1]
	v_pk_fma_f32 v[82:83], v[46:47], v[164:165], v[82:83] op_sel_hi:[0,1,1]
	v_pk_fma_f32 v[56:57], v[46:47], v[166:167], v[56:57] op_sel_hi:[0,1,1]
	v_pk_fma_f32 v[116:117], v[46:47], v[168:169], v[116:117] op_sel_hi:[0,1,1]
	v_pk_fma_f32 v[50:51], v[46:47], v[50:51], v[58:59] op_sel_hi:[0,1,1]
	v_pk_fma_f32 v[84:85], v[46:47], v[170:171], v[84:85] op_sel_hi:[0,1,1]
	v_pk_fma_f32 v[52:53], v[46:47], v[172:173], v[52:53] op_sel_hi:[0,1,1]
	v_pk_fma_f32 v[120:121], v[46:47], v[174:175], v[120:121] op_sel_hi:[0,1,1]
	v_pk_fma_f32 v[54:55], v[46:47], v[98:99], v[54:55] op_sel_hi:[0,1,1]
	v_pk_fma_f32 v[92:93], v[46:47], v[176:177], v[92:93] op_sel_hi:[0,1,1]
	v_pk_fma_f32 v[40:41], v[46:47], v[178:179], v[40:41] op_sel_hi:[0,1,1]
	v_pk_fma_f32 v[124:125], v[46:47], v[180:181], v[124:125] op_sel_hi:[0,1,1]
	v_pk_fma_f32 v[42:43], v[46:47], v[100:101], v[42:43] op_sel_hi:[0,1,1]
	v_add_f32_e32 v46, v134, v135
	s_waitcnt vmcnt(2)
	v_cvt_pk_f32_fp8_e32 v[188:189], v104
	v_pk_fma_f32 v[114:115], v[64:65], v[186:187], v[114:115] op_sel_hi:[0,1,1]
	v_add_f32_e32 v46, v46, v112
	v_pk_mul_f32 v[136:137], v[114:115], v[114:115]
	v_add_f32_e32 v46, v113, v46
	v_cvt_pk_f32_fp8_sdwa v[190:191], v104 src0_sel:WORD_1
	v_pk_fma_f32 v[62:63], v[64:65], v[102:103], v[62:63] op_sel_hi:[0,1,1]
	v_add_f32_e32 v46, v136, v46
	v_pk_mul_f32 v[80:81], v[62:63], v[62:63]
	v_add_f32_e32 v46, v137, v46
	v_cvt_pk_f32_fp8_e32 v[192:193], v105
	v_pk_fma_f32 v[82:83], v[64:65], v[188:189], v[82:83] op_sel_hi:[0,1,1]
	v_add_f32_e32 v46, v80, v46
	v_pk_mul_f32 v[96:97], v[82:83], v[82:83]
	v_add_f32_e32 v46, v81, v46
	v_cvt_pk_f32_fp8_sdwa v[104:105], v105 src0_sel:WORD_1
	v_pk_fma_f32 v[56:57], v[64:65], v[190:191], v[56:57] op_sel_hi:[0,1,1]
	v_add_f32_e32 v46, v96, v46
	v_pk_mul_f32 v[102:103], v[56:57], v[56:57]
	v_add_f32_e32 v46, v97, v46
	s_waitcnt vmcnt(1)
	v_cvt_pk_f32_fp8_e32 v[194:195], v106
	v_pk_fma_f32 v[116:117], v[64:65], v[192:193], v[116:117] op_sel_hi:[0,1,1]
	v_add_f32_e32 v46, v102, v46
	v_pk_mul_f32 v[118:119], v[116:117], v[116:117]
	v_add_f32_e32 v46, v103, v46
	v_cvt_pk_f32_fp8_sdwa v[196:197], v106 src0_sel:WORD_1
	v_pk_fma_f32 v[50:51], v[64:65], v[104:105], v[50:51] op_sel_hi:[0,1,1]
	v_add_f32_e32 v46, v118, v46
	v_pk_mul_f32 v[58:59], v[50:51], v[50:51]
	v_add_f32_e32 v46, v119, v46
	v_cvt_pk_f32_fp8_e32 v[198:199], v107
	v_pk_fma_f32 v[84:85], v[64:65], v[194:195], v[84:85] op_sel_hi:[0,1,1]
	v_add_f32_e32 v46, v58, v46
	v_pk_mul_f32 v[90:91], v[84:85], v[84:85]
	v_add_f32_e32 v46, v59, v46
	v_cvt_pk_f32_fp8_sdwa v[106:107], v107 src0_sel:WORD_1
	v_pk_fma_f32 v[52:53], v[64:65], v[196:197], v[52:53] op_sel_hi:[0,1,1]
	v_add_f32_e32 v46, v90, v46
	v_pk_mul_f32 v[104:105], v[52:53], v[52:53]
	v_add_f32_e32 v46, v91, v46
	s_waitcnt vmcnt(0)
	v_cvt_pk_f32_fp8_e32 v[200:201], v108
	v_pk_fma_f32 v[120:121], v[64:65], v[198:199], v[120:121] op_sel_hi:[0,1,1]
	v_add_f32_e32 v46, v104, v46
	v_pk_mul_f32 v[122:123], v[120:121], v[120:121]
	v_add_f32_e32 v46, v105, v46
	v_cvt_pk_f32_fp8_sdwa v[202:203], v108 src0_sel:WORD_1
	v_pk_fma_f32 v[54:55], v[64:65], v[106:107], v[54:55] op_sel_hi:[0,1,1]
	v_add_f32_e32 v46, v122, v46
	v_pk_mul_f32 v[86:87], v[54:55], v[54:55]
	v_add_f32_e32 v46, v123, v46
	v_cvt_pk_f32_fp8_e32 v[204:205], v109
	v_pk_fma_f32 v[92:93], v[64:65], v[200:201], v[92:93] op_sel_hi:[0,1,1]
	v_add_f32_e32 v46, v86, v46
	v_pk_mul_f32 v[98:99], v[92:93], v[92:93]
	v_add_f32_e32 v46, v87, v46
	v_cvt_pk_f32_fp8_sdwa v[108:109], v109 src0_sel:WORD_1
	v_pk_fma_f32 v[106:107], v[64:65], v[202:203], v[40:41] op_sel_hi:[0,1,1]
	v_add_f32_e32 v46, v98, v46
	v_pk_mul_f32 v[40:41], v[106:107], v[106:107]
	v_add_f32_e32 v46, v99, v46
	v_pk_fma_f32 v[124:125], v[64:65], v[204:205], v[124:125] op_sel_hi:[0,1,1]
	v_add_f32_e32 v40, v40, v46
	v_pk_mul_f32 v[126:127], v[124:125], v[124:125]
	v_add_f32_e32 v40, v41, v40
	v_pk_fma_f32 v[44:45], v[64:65], v[108:109], v[42:43] op_sel_hi:[0,1,1]
	v_add_f32_e32 v40, v126, v40
	v_pk_mul_f32 v[42:43], v[44:45], v[44:45]
	v_add_f32_e32 v40, v127, v40
	v_add_f32_e32 v40, v42, v40
	v_add_f32_e32 v40, v43, v40
	ds_bpermute_b32 v41, v73, v40
	s_waitcnt lgkmcnt(0)
	v_add_f32_e32 v40, v40, v41
	ds_bpermute_b32 v41, v74, v40
	s_waitcnt lgkmcnt(0)
	v_add_f32_e32 v40, v40, v41
	ds_bpermute_b32 v41, v75, v40
	s_waitcnt lgkmcnt(0)
	v_add_f32_e32 v40, v40, v41
	ds_bpermute_b32 v41, v76, v40
	s_waitcnt lgkmcnt(0)
	v_add_f32_e32 v40, v40, v41
	ds_bpermute_b32 v41, v77, v40
	s_waitcnt lgkmcnt(0)
	v_add_f32_e32 v40, v40, v41
	ds_bpermute_b32 v41, v78, v40
	s_waitcnt lgkmcnt(0)
	v_add_f32_e32 v40, v40, v41
	v_fmamk_f32 v40, v40, 0x3a000000, v72
	v_mul_f32_e32 v41, 0x4b800000, v40
	v_cmp_gt_f32_e32 vcc, s28, v40
	s_nop 1
	v_cndmask_b32_e32 v40, v40, v41, vcc
	v_rsq_f32_e32 v40, v40
	s_nop 0
	v_mul_f32_e32 v41, 0x45800000, v40
	v_cndmask_b32_e32 v46, v40, v41, vcc
	v_pk_mul_f32 v[40:41], v[110:111], v[46:47] op_sel_hi:[1,0]
	v_pk_mul_f32 v[42:43], v[60:61], v[46:47] op_sel_hi:[1,0]
	v_pk_mul_f32 v[40:41], v[4:5], v[40:41]
	v_pk_mul_f32 v[42:43], v[6:7], v[42:43]
	global_store_dwordx4 v[68:69], v[40:43], off offset:-4096
	s_andn2_b64 vcc, exec, s[20:21]
	s_nop 0
	v_pk_mul_f32 v[40:41], v[114:115], v[46:47] op_sel_hi:[1,0]
	v_pk_mul_f32 v[42:43], v[62:63], v[46:47] op_sel_hi:[1,0]
	v_pk_mul_f32 v[40:41], v[0:1], v[40:41]
	v_pk_mul_f32 v[42:43], v[2:3], v[42:43]
	global_store_dwordx4 v[68:69], v[40:43], off offset:-4080
	s_nop 1
	v_pk_mul_f32 v[40:41], v[82:83], v[46:47] op_sel_hi:[1,0]
	v_pk_mul_f32 v[42:43], v[56:57], v[46:47] op_sel_hi:[1,0]
	v_pk_mul_f32 v[40:41], v[12:13], v[40:41]
	v_pk_mul_f32 v[42:43], v[14:15], v[42:43]
	global_store_dwordx4 v[68:69], v[40:43], off offset:-2048
	s_nop 1
	v_pk_mul_f32 v[40:41], v[116:117], v[46:47] op_sel_hi:[1,0]
	v_pk_mul_f32 v[42:43], v[50:51], v[46:47] op_sel_hi:[1,0]
	v_pk_mul_f32 v[40:41], v[8:9], v[40:41]
	v_pk_mul_f32 v[42:43], v[10:11], v[42:43]
	global_store_dwordx4 v[68:69], v[40:43], off offset:-2032
	v_mov_b64_e32 v[50:51], v[34:35]
	v_mov_b64_e32 v[48:49], v[32:33]
	v_pk_mul_f32 v[40:41], v[84:85], v[46:47] op_sel_hi:[1,0]
	v_pk_mul_f32 v[42:43], v[52:53], v[46:47] op_sel_hi:[1,0]
	v_pk_mul_f32 v[40:41], v[20:21], v[40:41]
	v_pk_mul_f32 v[42:43], v[22:23], v[42:43]
	global_store_dwordx4 v[68:69], v[40:43], off
	s_nop 1
	v_pk_mul_f32 v[40:41], v[120:121], v[46:47] op_sel_hi:[1,0]
	v_pk_mul_f32 v[42:43], v[54:55], v[46:47] op_sel_hi:[1,0]
	v_pk_mul_f32 v[40:41], v[16:17], v[40:41]
	v_pk_mul_f32 v[42:43], v[18:19], v[42:43]
	global_store_dwordx4 v[68:69], v[40:43], off offset:16
	s_nop 1
	v_pk_mul_f32 v[40:41], v[92:93], v[46:47] op_sel_hi:[1,0]
	v_pk_mul_f32 v[42:43], v[106:107], v[46:47] op_sel_hi:[1,0]
	v_pk_mul_f32 v[40:41], v[28:29], v[40:41]
	v_pk_mul_f32 v[42:43], v[30:31], v[42:43]
	global_store_dwordx4 v[68:69], v[40:43], off offset:2048
	s_nop 1
	v_pk_mul_f32 v[40:41], v[124:125], v[46:47] op_sel_hi:[1,0]
	v_pk_mul_f32 v[42:43], v[44:45], v[46:47] op_sel_hi:[1,0]
	v_pk_mul_f32 v[40:41], v[24:25], v[40:41]
	v_pk_mul_f32 v[42:43], v[26:27], v[42:43]
	v_mov_b64_e32 v[46:47], v[38:39]
	global_store_dwordx4 v[68:69], v[40:43], off offset:2064
	v_lshl_add_u64 v[68:69], v[68:69], 0, s[14:15]
	v_mov_b64_e32 v[44:45], v[36:37]
	s_cbranch_vccz .LBB0_1104
.LBB0_1102:
	s_add_i32 s8, s8, s12
	s_cmpk_gt_i32 s8, 0x3fff
	s_cselect_b64 s[20:21], -1, 0
	s_and_b64 vcc, exec, s[20:21]
	s_cbranch_vccnz .LBB0_1101
	s_ashr_i32 s17, s16, 31
	s_lshl_b64 s[0:1], s[16:17], 2
	s_add_u32 s2, s24, s0
	s_addc_u32 s3, s25, s1
	s_add_u32 s30, s22, s0
	s_addc_u32 s31, s23, s1
	s_add_u32 s0, s26, s0
	s_addc_u32 s1, s27, s1
	global_load_dwordx4 v[208:211], v65, s[30:31]
	global_load_dwordx4 v[32:35], v65, s[2:3]
	global_load_dwordx4 v[36:39], v65, s[0:1]
	s_branch .LBB0_1101
